# P5: half of the workgroups (m-tile class) start ~16us late so HBM-bound out-proj epilogues interleave with the other half's K-loops
# speedup vs baseline: 1.0004x; 1.0004x over previous
; __device__ __forceinline__ bool tile_order(long L, int nM, int nN, int& pm, int& pn) {
;     const int nwg = nM * nN; if (L >= nwg) return false;
;     int wgid = (int)L; { const int q = nwg / 8, r = nwg % 8, xcd = wgid % 8, off = wgid / 8; wgid = (xcd < r ? xcd * (q + 1) : r * (q + 1) + (xcd - r) * q) + off; }
;     const int nig = WGM * nN, gid = wgid / nig, fm = gid * WGM, gsz = (nM - fm) < WGM ? (nM - fm) : WGM;
;     pm = fm + ((wgid % nig) % gsz); pn = (wgid % nig) / gsz; return true;
; __global__ void __launch_bounds__(NTHREADS, 2) hymba_fwd(Params p) {
;     ...
;     if (IN(5)) {
;         EpiOutProj E{p.x, (bf16*)(p.ws + WS_X1), (float*)(p.ws + WS_SSQ)};
;     ...
;         if (p.variant) { pg8::SchedDenseT<PROBE_CRIP5, OUTPROJ_F8 != 0> S{(const char*)(p.ws + WS_MIX), (const char*)(p.ws + WS_WOUT), T / 256, D / 256, G, cid};
;             pg8::gemm_phase<EpiOutProj, pg8::SchedDenseT<PROBE_CRIP5, OUTPROJ_F8 != 0>>(lds, S, E); } else
;     ...
;         { pg8::SchedDenseT<0, OUTPROJ_F8 != 0> S{(const char*)(p.ws + WS_MIX), (const char*)(p.ws + WS_WOUT), T / 256, D / 256, G, cid};
;           pg8::gemm_phase<EpiOutProj, pg8::SchedDenseT<0, OUTPROJ_F8 != 0>>(lds, S, E); }
.LBB0_552:
	s_cmp_lt_i32 s48, 6
	s_cselect_b64 s[4:5], -1, 0
	s_and_b64 s[0:1], s[4:5], s[0:1]
	s_andn2_b64 vcc, exec, s[0:1]
	s_cbranch_vccnz .LBB0_595
	s_bfe_u32 s98, s77, 0x10004
	s_cmp_eq_u32 s98, 0
	s_cbranch_scc1 .Lp5_nodelay
	s_mov_b32 s98, 4
.Lp5_delay:
	s_sleep 127
	s_sub_i32 s98, s98, 1
	s_cmp_lg_u32 s98, 0
	s_cbranch_scc1 .Lp5_delay
.Lp5_nodelay:
	s_add_u32 s2, s88, 0x3a800000
	s_addc_u32 s3, s89, 0
	s_add_u32 s17, s88, 0x22000000
	s_addc_u32 s46, s89, 0
	s_cmpk_lt_i32 s77, 0x400
	s_cselect_b64 s[0:1], -1, 0
	s_cmpk_gt_i32 s77, 0x3ff
	v_readfirstlane_b32 s14, v0
	s_cbranch_scc1 .LBB0_556
	s_ashr_i32 s6, s77, 31
	s_lshr_b32 s6, s6, 29
	s_add_i32 s8, s77, s6
	s_and_b32 s6, s8, -8
	s_sub_i32 s9, s77, s6
	s_cmp_gt_i32 s9, -1
	s_cbranch_scc0 .LBB0_557
	s_lshl_b32 s10, s9, 7
	s_cbranch_execz .LBB0_558
	s_branch .LBB0_559
